# MLA fast88 loop: first QK MFMA of each half-iteration issued right after the hoisted K-fragment reads (before the DMA issue blocks and the exponentials)
# baseline (speedup 1.0000x reference)
; #define ALAS __attribute__((address_space(3)))
; #define MF_ISSUE_K(t, s) do { glds16(ksrc + (long)(t) * 64 * 512, (unsigned)__builtin_amdgcn_readfirstlane(kdst + (s) * KSLOT)); \
;         if (wid < 4) glds16(krsrc + (long)(t) * 64 * 32, (unsigned)__builtin_amdgcn_readfirstlane(krdst + (s) * KSLOT)); } while (0)
; #define MF_ISSUE_V(t, s) glds16(vsrc + (long)(t) * 64 * 512, (unsigned)__builtin_amdgcn_readfirstlane(vdst + (s) * VSLOT))
; #define MF_ISSUE_K(t, s) glds16(ks8 + (long)(t) * kst8, (unsigned)__builtin_amdgcn_readfirstlane(kdst + (s) * KSLOT))
; #define MF_ISSUE_V(t, s) glds16(vsrc + (long)(t) * 64 * 512, (unsigned)__builtin_amdgcn_readfirstlane(vdst + (s) * VSLOT))
; #define M8_KFRAG(dst, base, m, kh) do { const u32x4 lo_ = *(ALAS const u32x4*)((base) + (((m) * 2 + (kh)) * 2) * 1024), hi_ = *(ALAS const u32x4*)((base) + (((m) * 2 + (kh)) * 2 + 1) * 1024); \
;         dst = (v8i){(int)lo_.x, (int)lo_.y, (int)lo_.z, (int)lo_.w, (int)hi_.x, (int)hi_.y, (int)hi_.z, (int)hi_.w}; } while (0)
; #define MF_ISSUE_K(t, s) glds16(ks8 + (long)(t) * kst8, (unsigned)__builtin_amdgcn_readfirstlane(kdst + (s) * KSLOT))
; #define MF_ISSUE_V(t, s) do { if (wid < 4) glds16(vs8 + (long)(t) * 4096, (unsigned)__builtin_amdgcn_readfirstlane(vdst + (s) * 4096)); } while (0)
; __device__ __forceinline__ bool mla_unit_fast88(const Args& A, int b, int h, int qb, ALAS char* shm, const int tidb) {
;     ...
;         for (int p = 0; p < 2; ++p) {
;             const int t = t2 + p; f32x16 &C0 = cs[p][0], &C1 = cs[p][1], &N0 = cs[p ^ 1][0], &N1 = cs[p ^ 1][1];
;             const bool vis = !bailed && t <= cw;
;             const int ks1 = ks == 2 ? 0 : ks + 1, ks2 = ks1 == 2 ? 0 : ks1 + 1;
;             if (t + 2 < t_end) MF_ISSUE_K(t + 2, ks2);
;             if (t + 1 < t_end) MF_ISSUE_V(t + 1, vs ^ 1);
;             if (vis) {
;                 {
;                     ALAS const char* Ks_ = Kfr + ks1 * KSLOT;
;                     v8i kfa, kfb; M8_KFRAG(kfa, Ks_, 0, 0);
;                     M8_KFRAG(kfb, Ks_, 0, 1);
;                     mfma8_new(N0, kfa, qf0, negm, sa8, sb8);
.LBB0_649:
	s_add_i32 s2, s4, 1
	s_cmp_lg_u32 s4, 2
	s_cselect_b32 s4, s2, 0
	v_lshl_add_u32 v171, s4, 13, v157
	ds_read_b128 v[114:117], v171
	ds_read_b128 v[118:121], v171 offset:1024
	ds_read_b128 v[164:167], v171 offset:2048
	ds_read_b128 v[168:171], v171 offset:3072
	s_add_i32 s7, s5, -3
	s_cmp_gt_i32 s7, s47
	s_cbranch_scc1 .Lmla_e0
	s_waitcnt lgkmcnt(2)
	v_mfma_scale_f32_32x32x64_f8f6f4 v[98:113], v[114:121], v[130:137], v[66:81], v247, v253 op_sel_hi:[0,0,0]
.Lmla_e0:
	s_add_i32 s6, s5, -1
	s_cmp_lt_u32 s6, s0
	s_cselect_b64 s[2:3], -1, 0
	s_and_b64 vcc, exec, s[2:3]
	v_lshl_add_u64 v[152:153], v[146:147], 0, v[0:1]
	s_cbranch_vccz .LBB0_651
	s_lshl_b32 s7, s4, 13
	s_addk_i32 s7, 0x2000
	s_cmp_lg_u32 s4, 2
	s_cselect_b32 s7, s7, 0
	v_lshl_add_u64 v[158:159], v[146:147], 0, v[0:1]
	s_add_i32 s7, s7, s45
	s_mov_b32 s8, m0
	s_mov_b32 m0, s7
	s_nop 0
	global_load_lds_dwordx4 v[158:159], off
	s_mov_b32 m0, s8

; #define ALAS __attribute__((address_space(3)))
; __device__ __forceinline__ bool mla_unit_fast88(const Args& A, int b, int h, int qb, ALAS char* shm, const int tidb) {
;     ...
;             if (vis) {
;                 {
;                     ALAS const char* Ks_ = Kfr + ks1 * KSLOT;
;                     v8i kfa, kfb; M8_KFRAG(kfa, Ks_, 0, 0);
;                     M8_KFRAG(kfb, Ks_, 0, 1);
;                     mfma8_new(N0, kfa, qf0, negm, sa8, sb8);
; #pragma unroll
;                     for (int e = 0; e < 8; ++e) C0[e] = __builtin_amdgcn_exp2f(C0[e]);
;                     __builtin_amdgcn_sched_barrier(0);
;                     M8_KFRAG(kfa, Ks_, 1, 0);
;                     mfma8_new(N1, kfb, qf0, negm, sa8, sb8);
; #pragma unroll
;                     for (int e = 8; e < 16; ++e) C0[e] = __builtin_amdgcn_exp2f(C0[e]);
;                     __builtin_amdgcn_sched_barrier(0);
;                     M8_KFRAG(kfb, Ks_, 1, 1);
;                     mfma8_acc(N0, kfa, qf1, sa8, sb8);
; #pragma unroll
;                     for (int e = 0; e < 8; ++e) C1[e] = __builtin_amdgcn_exp2f(C1[e]);
;                     __builtin_amdgcn_sched_barrier(0);
;                     mfma8_acc(N1, kfb, qf1, sa8, sb8);
; #pragma unroll
;                     for (int e = 8; e < 16; ++e) C1[e] = __builtin_amdgcn_exp2f(C1[e]);
;                     __builtin_amdgcn_sched_barrier(0);
;                 }
;                 ALAS const char* vb_ = shm + L_V + vs * 4096 + lane * 16;
;                 v8i vf0, vf1;
;                 { const u32x4 a0 = *(ALAS const u32x4*)(vb_), a1 = *(ALAS const u32x4*)(vb_ + 1024), b0 = *(ALAS const u32x4*)(vb_ + 2048), b1 = *(ALAS const u32x4*)(vb_ + 3072);
;                   vf0 = (v8i){(int)a0.x, (int)a0.y, (int)a0.z, (int)a0.w, (int)a1.x, (int)a1.y, (int)a1.z, (int)a1.w}; vf1 = (v8i){(int)b0.x, (int)b0.y, (int)b0.z, (int)b0.w, (int)b1.x, (int)b1.y, (int)b1.z, (int)b1.w}; }
;                 v8i pf;
; #pragma unroll
;                 for (int kk = 0; kk < 4; ++kk) { const f32x16& cc_ = (kk < 2) ? C0 : C1; const int k8_ = 8 * (kk & 1);
;                     int w0_ = 0, w1_ = 0;
;                     w0_ = __builtin_amdgcn_cvt_pk_bf8_f32(cc_[k8_], cc_[k8_ + 1], w0_, false); w0_ = __builtin_amdgcn_cvt_pk_bf8_f32(cc_[k8_ + 2], cc_[k8_ + 3], w0_, true);
.LBB0_653:
	s_add_i32 s7, s5, -3
	s_cmp_gt_i32 s7, s47
	s_cbranch_scc1 .LBB0_655
	v_lshl_add_u32 v158, s4, 13, v157
	v_exp_f32_e32 v50, v50
	v_exp_f32_e32 v51, v51
	v_exp_f32_e32 v52, v52
	v_exp_f32_e32 v53, v53
	v_exp_f32_e32 v54, v54
	v_exp_f32_e32 v55, v55
	v_exp_f32_e32 v56, v56
	v_exp_f32_e32 v57, v57
	ds_read_b128 v[172:175], v158 offset:4096
	ds_read_b128 v[176:179], v158 offset:5120
	v_exp_f32_e32 v58, v58
	v_exp_f32_e32 v59, v59
	v_exp_f32_e32 v60, v60
	v_exp_f32_e32 v61, v61
	v_exp_f32_e32 v62, v62
	v_exp_f32_e32 v63, v63
	v_exp_f32_e32 v64, v64
	v_exp_f32_e32 v65, v65
	s_waitcnt lgkmcnt(2)
	v_mfma_scale_f32_32x32x64_f8f6f4 v[114:129], v[164:171], v[130:137], v[66:81], v247, v253 op_sel_hi:[0,0,0]
	ds_read_b128 v[164:167], v158 offset:6144
	ds_read_b128 v[168:171], v158 offset:7168
	v_exp_f32_e32 v82, v82
	v_exp_f32_e32 v83, v83
	v_exp_f32_e32 v84, v84
	v_exp_f32_e32 v85, v85
	v_exp_f32_e32 v86, v86
	v_exp_f32_e32 v87, v87
	v_exp_f32_e32 v88, v88
	v_exp_f32_e32 v89, v89
	s_waitcnt lgkmcnt(2)
	v_mfma_scale_f32_32x32x64_f8f6f4 v[98:113], v[172:179], v[138:145], v[98:113], v247, v253 op_sel_hi:[0,0,0]
	v_exp_f32_e32 v90, v90
	v_exp_f32_e32 v91, v91
	v_exp_f32_e32 v92, v92
	v_exp_f32_e32 v93, v93
	v_exp_f32_e32 v94, v94
	v_exp_f32_e32 v95, v95
	v_exp_f32_e32 v96, v96
	v_exp_f32_e32 v97, v97
	s_waitcnt lgkmcnt(0)
	v_mfma_scale_f32_32x32x64_f8f6f4 v[114:129], v[164:171], v[138:145], v[114:129], v247, v253 op_sel_hi:[0,0,0]
	ds_read_b128 v[164:167], v157 offset:36864
	ds_read_b128 v[168:171], v157 offset:37888
	ds_read_b128 v[172:175], v157 offset:38912
	ds_read_b128 v[176:179], v157 offset:39936
	v_mov_b32_e32 v180, 0
	v_mov_b32_e32 v181, 0
	v_mov_b32_e32 v182, 0
	v_mov_b32_e32 v183, 0
	v_mov_b32_e32 v184, 0
	v_mov_b32_e32 v185, 0
	v_mov_b32_e32 v186, 0
	v_mov_b32_e32 v187, 0
	v_cvt_pk_bf8_f32 v180, v50, v51
	v_cvt_pk_bf8_f32 v181, v54, v55
	v_cvt_pk_bf8_f32 v182, v58, v59
	v_cvt_pk_bf8_f32 v183, v62, v63
	v_cvt_pk_bf8_f32 v184, v82, v83
	v_cvt_pk_bf8_f32 v185, v86, v87
	v_cvt_pk_bf8_f32 v186, v90, v91
	v_cvt_pk_bf8_f32 v187, v94, v95
	v_cvt_pk_bf8_f32 v180, v52, v53 op_sel:[0,0,1]
	v_cvt_pk_bf8_f32 v181, v56, v57 op_sel:[0,0,1]
	v_cvt_pk_bf8_f32 v182, v60, v61 op_sel:[0,0,1]
	v_cvt_pk_bf8_f32 v183, v64, v65 op_sel:[0,0,1]
	v_cvt_pk_bf8_f32 v184, v84, v85 op_sel:[0,0,1]
	v_cvt_pk_bf8_f32 v185, v88, v89 op_sel:[0,0,1]
	v_cvt_pk_bf8_f32 v186, v92, v93 op_sel:[0,0,1]
	v_cvt_pk_bf8_f32 v187, v96, v97 op_sel:[0,0,1]
	s_waitcnt lgkmcnt(2)
	v_mfma_scale_f32_32x32x64_f8f6f4 v[2:17], v[180:187], v[164:171], v[2:17], v251, v247 op_sel_hi:[0,0,0] cbsz:1
	s_waitcnt lgkmcnt(0)
	v_mfma_scale_f32_32x32x64_f8f6f4 v[18:33], v[180:187], v[172:179], v[18:33], v251, v247 op_sel_hi:[0,0,0] cbsz:1
	v_mov_b32_e32 v163, v162
	v_mov_b32_e32 v164, v162
	v_mov_b32_e32 v165, v162
	v_mov_b32_e32 v166, v162
	v_mov_b32_e32 v167, v162
	v_mov_b32_e32 v168, v162
	v_mov_b32_e32 v169, v162
	v_mfma_scale_f32_32x32x64_f8f6f4 v[34:49], v[180:187], v[162:169], v[34:49], v251, v251 op_sel_hi:[0,0,0] cbsz:1
.LBB0_655:
	s_add_i32 s8, s4, 1
	s_waitcnt vmcnt(0) lgkmcnt(0)
	s_barrier
	s_cmp_lg_u32 s4, 2
	s_cselect_b32 s4, s8, 0
	v_lshl_add_u32 v171, s4, 13, v157
	ds_read_b128 v[82:85], v171
	ds_read_b128 v[86:89], v171 offset:1024
	ds_read_b128 v[164:167], v171 offset:2048
	ds_read_b128 v[168:171], v171 offset:3072
	s_cmp_ge_i32 s7, s47
	s_cbranch_scc1 .Lmla_e1
	s_waitcnt lgkmcnt(2)
	v_mfma_scale_f32_32x32x64_f8f6f4 v[50:65], v[82:89], v[130:137], v[66:81], v247, v253 op_sel_hi:[0,0,0]
.Lmla_e1:
	s_cmp_ge_u32 s5, s0
	s_cbranch_scc1 .LBB0_661
	s_lshl_b32 s8, s4, 13
	s_addk_i32 s8, 0x2000
	s_cmp_lg_u32 s4, 2
	s_cselect_b32 s8, s8, 0
	v_lshl_add_u64 v[146:147], v[146:147], 0, v[148:149]
	s_add_i32 s8, s8, s45
	s_mov_b32 s9, m0
	s_mov_b32 m0, s8
	s_nop 0
	global_load_lds_dwordx4 v[146:147], off
	s_mov_b32 m0, s9
	s_and_b64 s[2:3], s[34:35], s[2:3]
	s_andn2_b64 vcc, exec, s[2:3]
	s_cbranch_vccz .LBB0_662

; #define ALAS __attribute__((address_space(3)))
; __device__ __forceinline__ bool mla_unit_fast88(const Args& A, int b, int h, int qb, ALAS char* shm, const int tidb) {
;     ...
;             if (vis) {
;                 {
;                     ALAS const char* Ks_ = Kfr + ks1 * KSLOT;
;                     v8i kfa, kfb; M8_KFRAG(kfa, Ks_, 0, 0);
;                     M8_KFRAG(kfb, Ks_, 0, 1);
;                     mfma8_new(N0, kfa, qf0, negm, sa8, sb8);
; #pragma unroll
;                     for (int e = 0; e < 8; ++e) C0[e] = __builtin_amdgcn_exp2f(C0[e]);
;                     __builtin_amdgcn_sched_barrier(0);
;                     M8_KFRAG(kfa, Ks_, 1, 0);
;                     mfma8_new(N1, kfb, qf0, negm, sa8, sb8);
; #pragma unroll
;                     for (int e = 8; e < 16; ++e) C0[e] = __builtin_amdgcn_exp2f(C0[e]);
;                     __builtin_amdgcn_sched_barrier(0);
;                     M8_KFRAG(kfb, Ks_, 1, 1);
;                     mfma8_acc(N0, kfa, qf1, sa8, sb8);
; #pragma unroll
;                     for (int e = 0; e < 8; ++e) C1[e] = __builtin_amdgcn_exp2f(C1[e]);
;                     __builtin_amdgcn_sched_barrier(0);
;                     mfma8_acc(N1, kfb, qf1, sa8, sb8);
; #pragma unroll
;                     for (int e = 8; e < 16; ++e) C1[e] = __builtin_amdgcn_exp2f(C1[e]);
;                     __builtin_amdgcn_sched_barrier(0);
;                 }
;                 ALAS const char* vb_ = shm + L_V + vs * 4096 + lane * 16;
;                 v8i vf0, vf1;
;                 { const u32x4 a0 = *(ALAS const u32x4*)(vb_), a1 = *(ALAS const u32x4*)(vb_ + 1024), b0 = *(ALAS const u32x4*)(vb_ + 2048), b1 = *(ALAS const u32x4*)(vb_ + 3072);
;                   vf0 = (v8i){(int)a0.x, (int)a0.y, (int)a0.z, (int)a0.w, (int)a1.x, (int)a1.y, (int)a1.z, (int)a1.w}; vf1 = (v8i){(int)b0.x, (int)b0.y, (int)b0.z, (int)b0.w, (int)b1.x, (int)b1.y, (int)b1.z, (int)b1.w}; }
;                 v8i pf;
; #pragma unroll
;                 for (int kk = 0; kk < 4; ++kk) { const f32x16& cc_ = (kk < 2) ? C0 : C1; const int k8_ = 8 * (kk & 1);
;                     int w0_ = 0, w1_ = 0;
;                     w0_ = __builtin_amdgcn_cvt_pk_bf8_f32(cc_[k8_], cc_[k8_ + 1], w0_, false); w0_ = __builtin_amdgcn_cvt_pk_bf8_f32(cc_[k8_ + 2], cc_[k8_ + 3], w0_, true);
.LBB0_658:
	v_lshl_add_u32 v146, s4, 13, v157
	v_exp_f32_e32 v98, v98
	v_exp_f32_e32 v99, v99
	v_exp_f32_e32 v100, v100
	v_exp_f32_e32 v101, v101
	v_exp_f32_e32 v102, v102
	v_exp_f32_e32 v103, v103
	v_exp_f32_e32 v104, v104
	v_exp_f32_e32 v105, v105
	ds_read_b128 v[172:175], v146 offset:4096
	ds_read_b128 v[176:179], v146 offset:5120
	v_exp_f32_e32 v106, v106
	v_exp_f32_e32 v107, v107
	v_exp_f32_e32 v108, v108
	v_exp_f32_e32 v109, v109
	v_exp_f32_e32 v110, v110
	v_exp_f32_e32 v111, v111
	v_exp_f32_e32 v112, v112
	v_exp_f32_e32 v113, v113
	s_waitcnt lgkmcnt(2)
	v_mfma_scale_f32_32x32x64_f8f6f4 v[82:97], v[164:171], v[130:137], v[66:81], v247, v253 op_sel_hi:[0,0,0]
	ds_read_b128 v[164:167], v146 offset:6144
	ds_read_b128 v[168:171], v146 offset:7168
	v_exp_f32_e32 v114, v114
	v_exp_f32_e32 v115, v115
	v_exp_f32_e32 v116, v116
	v_exp_f32_e32 v117, v117
	v_exp_f32_e32 v118, v118
	v_exp_f32_e32 v119, v119
	v_exp_f32_e32 v120, v120
	v_exp_f32_e32 v121, v121
	s_waitcnt lgkmcnt(2)
	v_mfma_scale_f32_32x32x64_f8f6f4 v[50:65], v[172:179], v[138:145], v[50:65], v247, v253 op_sel_hi:[0,0,0]
	v_exp_f32_e32 v122, v122
	v_exp_f32_e32 v123, v123
	v_exp_f32_e32 v124, v124
	v_exp_f32_e32 v125, v125
	v_exp_f32_e32 v126, v126
	v_exp_f32_e32 v127, v127
	v_exp_f32_e32 v128, v128
	v_exp_f32_e32 v129, v129
	s_waitcnt lgkmcnt(0)
	v_mfma_scale_f32_32x32x64_f8f6f4 v[82:97], v[164:171], v[138:145], v[82:97], v247, v253 op_sel_hi:[0,0,0]
	ds_read_b128 v[164:167], v157 offset:40960
	ds_read_b128 v[168:171], v157 offset:41984
	ds_read_b128 v[172:175], v157 offset:43008
	ds_read_b128 v[176:179], v157 offset:44032
	v_mov_b32_e32 v180, 0
	v_mov_b32_e32 v181, 0
	v_mov_b32_e32 v182, 0
	v_mov_b32_e32 v183, 0
	v_mov_b32_e32 v184, 0
	v_mov_b32_e32 v185, 0
	v_mov_b32_e32 v186, 0
	v_mov_b32_e32 v187, 0
	v_cvt_pk_bf8_f32 v180, v98, v99
	v_cvt_pk_bf8_f32 v181, v102, v103
	v_cvt_pk_bf8_f32 v182, v106, v107
	v_cvt_pk_bf8_f32 v183, v110, v111
	v_cvt_pk_bf8_f32 v184, v114, v115
	v_cvt_pk_bf8_f32 v185, v118, v119
	v_cvt_pk_bf8_f32 v186, v122, v123
	v_cvt_pk_bf8_f32 v187, v126, v127
	v_cvt_pk_bf8_f32 v180, v100, v101 op_sel:[0,0,1]
	v_cvt_pk_bf8_f32 v181, v104, v105 op_sel:[0,0,1]
	v_cvt_pk_bf8_f32 v182, v108, v109 op_sel:[0,0,1]
	v_cvt_pk_bf8_f32 v183, v112, v113 op_sel:[0,0,1]
	v_cvt_pk_bf8_f32 v184, v116, v117 op_sel:[0,0,1]
	v_cvt_pk_bf8_f32 v185, v120, v121 op_sel:[0,0,1]
	v_cvt_pk_bf8_f32 v186, v124, v125 op_sel:[0,0,1]
	v_cvt_pk_bf8_f32 v187, v128, v129 op_sel:[0,0,1]
	s_waitcnt lgkmcnt(2)
	v_mfma_scale_f32_32x32x64_f8f6f4 v[2:17], v[180:187], v[164:171], v[2:17], v251, v247 op_sel_hi:[0,0,0] cbsz:1
	s_waitcnt lgkmcnt(0)
	v_mfma_scale_f32_32x32x64_f8f6f4 v[18:33], v[180:187], v[172:179], v[18:33], v251, v247 op_sel_hi:[0,0,0] cbsz:1
	v_mov_b32_e32 v163, v162
	v_mov_b32_e32 v164, v162
	v_mov_b32_e32 v165, v162
	v_mov_b32_e32 v166, v162
	v_mov_b32_e32 v167, v162
	v_mov_b32_e32 v168, v162
	v_mov_b32_e32 v169, v162
	v_mfma_scale_f32_32x32x64_f8f6f4 v[34:49], v[180:187], v[162:169], v[34:49], v251, v251 op_sel_hi:[0,0,0] cbsz:1
